# speedup vs baseline: 1.0018x; 1.0018x over previous
.Lep1_end:
	v_mov_b32_e32 v2, v0
	v_ashrrev_i32_e32 v3, 5, v2
	v_lshlrev_b32_e32 v2, 4, v2
	v_and_b32_e32 v2, 0x1f0, v2
	v_min_i32_e32 v4, 0x53, v3
	v_lshl_or_b32 v4, v4, 9, v2
	v_min_i32_e32 v5, 0x43, v3
	v_lshl_or_b32 v5, v5, 9, v2
	v_min_i32_e32 v6, 51, v3
	v_lshl_or_b32 v6, v6, 9, v2
	v_min_i32_e32 v7, 35, v3
	v_lshl_or_b32 v7, v7, 9, v2
	v_min_i32_e32 v8, 19, v3
	v_lshl_or_b32 v8, v8, 9, v2
	v_min_i32_e32 v3, 3, v3
	v_lshl_or_b32 v2, v3, 9, v2
	s_waitcnt lgkmcnt(0)
	s_barrier
	s_lshl_b32 s30, s36, 1
	ds_read_b128 v[54:57], v4
	ds_read_b128 v[50:53], v5 offset:8192
	ds_read_b128 v[46:49], v6 offset:16384
	ds_read_b128 v[42:45], v7 offset:24576
	ds_read_b128 v[38:41], v8 offset:32768
	ds_read_b128 v[34:37], v2 offset:40960
	s_lshl_b64 s[26:27], s[36:37], 17
	v_lshl_add_u64 v[2:3], v[212:213], 0, s[26:27]
	v_add_co_u32_e32 v4, vcc, s65, v2
	global_load_dwordx4 v[100:103], v[2:3], off
	global_load_dwordx4 v[92:95], v[2:3], off offset:1024
	global_load_dwordx4 v[88:91], v[2:3], off offset:2048
	global_load_dwordx4 v[80:83], v[2:3], off offset:3072
	v_addc_co_u32_e32 v5, vcc, 0, v3, vcc
	v_add_co_u32_e32 v6, vcc, s75, v2
	s_lshl_b32 s26, s36, 9
	s_nop 0
	v_addc_co_u32_e32 v7, vcc, 0, v3, vcc
	v_add_co_u32_e32 v2, vcc, s66, v2
	s_mov_b32 s27, s37
	s_nop 0
	v_addc_co_u32_e32 v3, vcc, 0, v3, vcc
	v_lshl_add_u64 v[14:15], s[26:27], 2, v[218:219]
	global_load_dwordx4 v[84:87], v[4:5], off offset:1024
	global_load_dwordx4 v[76:79], v[4:5], off offset:2048
	global_load_dwordx4 v[96:99], v[6:7], off offset:-4096
	global_load_dwordx4 v[128:131], v[6:7], off
	global_load_dwordx4 v[124:127], v[6:7], off offset:1024
	global_load_dwordx4 v[120:123], v[6:7], off offset:2048
	global_load_dwordx4 v[112:115], v[6:7], off offset:3072
	global_load_dwordx4 v[68:71], v[4:5], off offset:3072
	global_load_dwordx4 v[116:119], v[2:3], off
	global_load_dwordx4 v[108:111], v[2:3], off offset:1024
	global_load_dwordx4 v[104:107], v[2:3], off offset:2048
	global_load_dwordx4 v[72:75], v[2:3], off offset:3072
	global_load_dwordx4 v[18:21], v[14:15], off offset:1536
	global_load_dwordx4 v[22:25], v[14:15], off offset:1568
	s_nop 0
	global_load_dwordx4 v[2:5], v[14:15], off offset:1664
	global_load_dwordx4 v[6:9], v[14:15], off offset:1696
	global_load_dwordx4 v[26:29], v[14:15], off offset:1600
	global_load_dwordx4 v[30:33], v[14:15], off offset:1632
	global_load_dwordx4 v[10:13], v[14:15], off offset:1728
	s_nop 0
	global_load_dwordx4 v[14:17], v[14:15], off offset:1760
	v_mov_b32_e32 v58, v0
	s_or_b32 s80, s30, 1
	s_lshl_b32 s26, s36, 7
	s_nop 0
	v_cmp_gt_i32_e32 vcc, s76, v58
	s_and_saveexec_b64 s[30:31], vcc
	s_cbranch_execz .LBB1_126
	s_lshl_b64 s[40:41], s[26:27], 2
	s_add_u32 s40, s22, s40
	s_addc_u32 s41, s23, s41
	v_and_b32_e32 v58, 63, v0
	v_lshrrev_b32_e32 v64, 6, v0
	v_lshrrev_b32_e32 v59, 3, v58
	v_and_b32_e32 v60, 7, v58
	v_readfirstlane_b32 s52, v64
	v_min_u32_e32 v61, 4, v59
	v_lshlrev_b32_e32 v62, 6, v61
	v_lshl_add_u32 v62, v60, 3, v62
	v_mul_u32_u24_e32 v63, 7, v61
	v_add_u32_e32 v63, v63, v60
	v_cmp_gt_u32_e64 s[46:47], 5, v59
	v_cmp_gt_u32_e64 s[48:49], 7, v60
	v_cmp_gt_u32_e32 vcc, 32, v63
	v_cmp_eq_u32_e64 s[50:51], 7, v60
	s_and_b64 s[46:47], s[46:47], s[48:49]
	s_and_b64 s[46:47], s[46:47], vcc
	v_min_u32_e32 v63, 31, v63
	v_lshl_add_u32 v63, v64, 5, v63
	v_lshlrev_b32_e32 v65, 2, v63
	global_load_dword v132, v65, s[40:41]
	v_lshl_add_u32 v133, v63, 2, v249
	s_mul_i32 s52, s52, 0x140
	s_mul_i32 s53, s36, 0x5000
	s_add_i32 s53, s53, s52
	s_add_u32 s42, s18, s53
	s_addc_u32 s43, s19, 0
	s_add_u32 s44, s42, 0x1400
	s_addc_u32 s45, s43, 0
	s_mov_b32 s82, 0x10000
	s_mov_b32 s81, 0x42000000

.Lep2_end:
	v_mov_b32_e32 v2, v0
	v_ashrrev_i32_e32 v3, 5, v2
	v_lshlrev_b32_e32 v2, 4, v2
	v_and_b32_e32 v2, 0x1f0, v2
	v_min_i32_e32 v4, 0x53, v3
	v_lshl_or_b32 v4, v4, 9, v2
	v_min_i32_e32 v5, 0x43, v3
	v_lshl_or_b32 v5, v5, 9, v2
	v_min_i32_e32 v6, 51, v3
	v_lshl_or_b32 v6, v6, 9, v2
	v_min_i32_e32 v7, 35, v3
	v_lshl_or_b32 v7, v7, 9, v2
	v_min_i32_e32 v8, 19, v3
	v_lshl_or_b32 v8, v8, 9, v2
	v_min_i32_e32 v3, 3, v3
	v_lshl_or_b32 v2, v3, 9, v2
	s_waitcnt lgkmcnt(0)
	s_barrier
	s_nop 0
	ds_read_b128 v[42:45], v4
	ds_read_b128 v[38:41], v5 offset:8192
	ds_read_b128 v[34:37], v6 offset:16384
	ds_read_b128 v[30:33], v7 offset:24576
	ds_read_b128 v[22:25], v8 offset:32768
	ds_read_b128 v[18:21], v2 offset:40960
	s_add_i32 s80, s36, 1
	s_cmp_lg_u32 s36, 2
	s_cselect_b64 s[30:31], -1, 0
	s_and_b64 s[40:41], s[30:31], exec
	s_cselect_b32 s42, s80, 2
	s_lshl_b32 s40, s42, 15
	s_mov_b32 s41, s37
	v_lshl_add_u64 v[2:3], v[196:197], 0, s[40:41]
	v_lshl_add_u64 v[4:5], v[198:199], 0, s[40:41]
	v_lshl_add_u64 v[6:7], v[200:201], 0, s[40:41]
	global_load_dwordx4 v[116:119], v[2:3], off
	global_load_dwordx4 v[120:123], v[2:3], off offset:1024
	global_load_dwordx4 v[112:115], v[4:5], off
	global_load_dwordx4 v[100:103], v[4:5], off offset:1024
	global_load_dwordx4 v[96:99], v[6:7], off
	global_load_dwordx4 v[76:79], v[6:7], off offset:1024
	global_load_dwordx4 v[124:127], v[2:3], off offset:2048
	global_load_dwordx4 v[128:131], v[2:3], off offset:3072
	global_load_dwordx4 v[104:107], v[4:5], off offset:2048
	global_load_dwordx4 v[108:111], v[4:5], off offset:3072
	global_load_dwordx4 v[72:75], v[6:7], off offset:2048
	global_load_dwordx4 v[68:71], v[6:7], off offset:3072
	v_add_co_u32_e32 v2, vcc, s65, v2
	s_lshl_b32 s40, s42, 7
	s_nop 0
	v_addc_co_u32_e32 v3, vcc, 0, v3, vcc
	v_add_co_u32_e32 v4, vcc, s65, v4
	v_lshl_add_u64 v[14:15], s[40:41], 2, v[202:203]
	s_nop 0
	v_addc_co_u32_e32 v5, vcc, 0, v5, vcc
	v_add_co_u32_e32 v6, vcc, s65, v6
	s_nop 1
	v_addc_co_u32_e32 v7, vcc, 0, v7, vcc
	global_load_dwordx4 v[148:151], v[2:3], off
	global_load_dwordx4 v[152:155], v[2:3], off offset:1024
	global_load_dwordx4 v[132:135], v[4:5], off
	global_load_dwordx4 v[136:139], v[4:5], off offset:1024
	global_load_dwordx4 v[92:95], v[6:7], off
	global_load_dwordx4 v[84:87], v[6:7], off offset:1024
	global_load_dwordx4 v[156:159], v[2:3], off offset:2048
	global_load_dwordx4 v[160:163], v[2:3], off offset:3072
	global_load_dwordx4 v[140:143], v[4:5], off offset:2048
	global_load_dwordx4 v[144:147], v[4:5], off offset:3072
	global_load_dwordx4 v[88:91], v[6:7], off offset:2048
	global_load_dwordx4 v[80:83], v[6:7], off offset:3072
	s_nop 0
	global_load_dwordx4 v[2:5], v[14:15], off
	global_load_dwordx4 v[6:9], v[14:15], off offset:32
	global_load_dwordx4 v[10:13], v[14:15], off offset:64
	s_nop 0
	global_load_dwordx4 v[14:17], v[14:15], off offset:96
	s_nop 0
	global_load_dwordx4 v[26:29], v[216:217], off offset:1024
	v_mov_b32_e32 v46, v0
	s_nop 0
	v_cmp_gt_i32_e32 vcc, s76, v46
	s_and_saveexec_b64 s[40:41], vcc
	s_cbranch_execz .LBB1_207
	s_lshl_b64 s[26:27], s[26:27], 2
	s_add_u32 s26, s24, s26
	s_addc_u32 s27, s25, s27
	v_and_b32_e32 v46, 63, v0
	v_lshrrev_b32_e32 v52, 6, v0
	v_lshrrev_b32_e32 v47, 3, v46
	v_and_b32_e32 v48, 7, v46
	v_readfirstlane_b32 s52, v52
	v_min_u32_e32 v49, 4, v47
	v_lshlrev_b32_e32 v50, 6, v49
	v_lshl_add_u32 v50, v48, 3, v50
	v_mul_u32_u24_e32 v51, 7, v49
	v_add_u32_e32 v51, v51, v48
	v_cmp_gt_u32_e64 s[46:47], 5, v47
	v_cmp_gt_u32_e64 s[48:49], 7, v48
	v_cmp_gt_u32_e32 vcc, 32, v51
	v_cmp_eq_u32_e64 s[50:51], 7, v48
	s_and_b64 s[46:47], s[46:47], s[48:49]
	s_and_b64 s[46:47], s[46:47], vcc
	v_min_u32_e32 v51, 31, v51
	v_lshl_add_u32 v51, v52, 5, v51
	v_lshlrev_b32_e32 v53, 2, v51
	global_load_dword v54, v53, s[26:27]
	v_lshl_add_u32 v55, v51, 2, v249
	s_mul_i32 s52, s52, 0x140
	s_mul_i32 s53, s36, 0x5000
	s_addk_i32 s53, 0x2800
	s_add_i32 s53, s53, s52
	s_add_u32 s42, s18, s53
	s_addc_u32 s43, s19, 0
	s_add_u32 s44, s42, 0x1400
	s_addc_u32 s45, s43, 0
	s_mov_b32 s81, 0x10000
	s_mov_b32 s82, 0x42000000
